# nt hint on P6's A-operand (HM, last use) LDS-DMA loads
# speedup vs baseline: 1.0062x; 1.0062x over previous
.LBB0_642:
	v_lshlrev_b32_e32 v4, 4, v3
	s_movk_i32 s0, 0x70
	v_bitop3_b32 v4, v4, s0, v3 bitop3:0x48
	v_lshlrev_b32_e32 v3, 7, v3
	v_lshl_or_b32 v4, s37, 18, v4
	v_and_b32_e32 v3, 0xfffffc00, v3
	v_add_u32_e32 v162, v4, v3
	v_lshrrev_b32_e32 v3, 4, v2
	v_ashrrev_i32_e32 v5, 3, v2
	v_xor_b32_e32 v4, v3, v2
	v_lshlrev_b32_e32 v6, 1, v5
	v_lshrrev_b32_e32 v7, 2, v5
	v_lshlrev_b32_e32 v4, 4, v4
	v_and_b32_e32 v6, 24, v6
	v_and_b32_e32 v7, 4, v7
	v_and_b32_e32 v5, 0x3fffe3, v5
	v_and_b32_e32 v4, 0x70, v4
	v_or3_b32 v5, v5, v7, v6
	s_lshl_b32 s1, s5, 10
	s_ashr_i32 s22, s4, 8
	v_lshl_or_b32 v172, v5, 10, v4
	v_mov_b32_e32 v5, 0x2000
	s_add_i32 s1, s1, 0
	v_lshl_add_u32 v5, v2, 4, v5
	s_add_u32 s29, s10, 0x1c00000
	v_ashrrev_i32_e32 v5, 7, v5
	s_addc_u32 s31, s11, 0
	s_ashr_i32 s39, s38, 31
	v_lshlrev_b32_e32 v6, 1, v5
	v_lshrrev_b32_e32 v7, 2, v5
	s_lshl_b64 s[20:21], s[38:39], 18
	v_and_b32_e32 v6, 24, v6
	v_and_b32_e32 v7, 4, v7
	v_and_b32_e32 v5, 0x3fffe3, v5
	s_add_u32 s42, s29, s20
	v_or3_b32 v5, v5, v7, v6
	s_addc_u32 s43, s31, s21
	s_add_i32 s33, s1, 0x10000
	s_mov_b32 m0, s33
	s_nop 0
	global_load_lds_dwordx4 v172, s[42:43] offset:0
	v_lshl_or_b32 v173, v5, 10, v4
	s_add_i32 s39, s1, 0x12000
	s_mov_b32 m0, s39
	s_nop 0
	global_load_lds_dwordx4 v173, s[42:43] offset:0
	s_add_u32 s20, s42, 0x20000
	s_addc_u32 s21, s43, 0
	s_add_i32 s41, s1, 0x14000
	s_mov_b32 m0, s41
	s_nop 0
	global_load_lds_dwordx4 v172, s[20:21] offset:0
	s_add_i32 s48, s1, 0x16000
	s_mov_b32 m0, s48
	s_nop 0
	global_load_lds_dwordx4 v173, s[20:21] offset:0
	s_mov_b32 m0, s1
	s_nop 0
	global_load_lds_dwordx4 v162, s[12:13] offset:0 nt
	v_add_u32_e32 v170, 0x10000, v162
	s_add_i32 s49, s1, 0x2000
	s_mov_b32 m0, s49
	s_nop 0
	global_load_lds_dwordx4 v170, s[12:13] offset:0 nt
	v_add_u32_e32 v163, 0x20000, v162
	s_add_i32 s50, s1, 0x4000
	s_mov_b32 m0, s50
	s_nop 0
	global_load_lds_dwordx4 v163, s[12:13] offset:0 nt
	v_add_u32_e32 v171, 0x30000, v162
	s_add_i32 s51, s1, 0x6000
	s_mov_b32 m0, s51
	s_nop 0
	global_load_lds_dwordx4 v171, s[12:13] offset:0 nt
	s_cmp_eq_u32 s22, 1
	s_mov_b32 s63, 0
	s_cselect_b64 s[20:21], -1, 0
	s_cmp_lg_u32 s22, 1
	s_cbranch_scc1 .LBB0_644
	s_barrier
.LBB0_644:
	v_and_b32_e32 v4, 15, v2
	s_lshl_b32 s5, s5, 5
	v_lshlrev_b32_e32 v5, 7, v4
	s_and_b32 s5, s5, 0x60
	v_lshl_or_b32 v5, s22, 13, v5
	s_add_u32 s22, s42, 0x80
	v_or_b32_e32 v4, s5, v4
	s_waitcnt vmcnt(2)
	s_barrier
	s_addc_u32 s23, s43, 0
	s_add_i32 s52, s1, 0x18000
	s_mov_b32 m0, s52
	s_nop 0
	global_load_lds_dwordx4 v172, s[22:23] offset:0
	s_add_i32 s53, s1, 0x1a000
	s_mov_b32 m0, s53
	s_nop 0
	global_load_lds_dwordx4 v173, s[22:23] offset:0
	s_add_u32 s22, s12, 0x80
	s_addc_u32 s23, s13, 0
	s_add_i32 s54, s1, 0x8000
	s_mov_b32 m0, s54
	s_nop 0
	global_load_lds_dwordx4 v162, s[22:23] offset:0 nt
	s_add_i32 s55, s1, 0xa000
	s_mov_b32 m0, s55
	s_nop 0
	global_load_lds_dwordx4 v170, s[22:23] offset:0 nt
	s_add_u32 s24, s42, 0x20080
	s_addc_u32 s25, s43, 0
	s_add_i32 s56, s1, 0x1c000
	s_mov_b32 m0, s56
	s_nop 0
	global_load_lds_dwordx4 v172, s[24:25] offset:0
	s_add_i32 s57, s1, 0x1e000
	s_add_i32 s58, s1, 0xc000
	v_bfe_u32 v6, v2, 4, 2
	v_bfe_u32 v2, v2, 1, 3
	s_mov_b32 m0, s57
	s_nop 0
	global_load_lds_dwordx4 v173, s[24:25] offset:0
	s_add_u32 s24, s12, 0x380
	v_bitop3_b32 v3, v3, v2, 3 bitop3:0x6c
	v_bitop3_b32 v2, v6, v2, 4 bitop3:0x36
	s_addc_u32 s25, s13, 0
	v_lshlrev_b32_e32 v3, 4, v3
	v_lshlrev_b32_e32 v2, 4, v2
	v_lshlrev_b32_e32 v4, 7, v4
	s_cmpk_lt_u32 s4, 0x100
	v_or_b32_e32 v174, v4, v3
	v_or_b32_e32 v175, v4, v2
	s_waitcnt vmcnt(6)
	s_cselect_b64 s[26:27], -1, 0
	s_add_i32 s4, 0, 0x10000
	v_or_b32_e32 v7, v3, v5
	v_or_b32_e32 v5, v2, v5
	v_add_u32_e32 v176, s4, v174
	v_add_u32_e32 v177, s4, v175
	s_add_i32 s4, 0, 0x14000
	s_add_i32 s59, s1, 0xe000
	v_add_u32_e32 v178, s4, v174
	v_add_u32_e32 v179, s4, v175
	v_add_u32_e32 v180, 0, v7
	v_add_u32_e32 v181, 0, v5
	v_mov_b32_e32 v182, 0x7f7f7f7f
	s_mov_b32 s28, 0x42000000
	s_movk_i32 s60, 0xffc0
	s_mov_b32 s30, 0x3c800000
	s_barrier
	s_branch .LBB0_647

.LBB0_649:
	s_mov_b32 s35, -2
	.p2align 3
	s_nop 0
	ds_read_b128 v[18:21], v176
	ds_read_b128 v[26:29], v176 offset:2048
	ds_read_b128 v[22:25], v177
	ds_read_b128 v[30:33], v177 offset:2048
	ds_read_b128 v[2:5], v178
	ds_read_b128 v[10:13], v178 offset:2048
	ds_read_b128 v[6:9], v179
	ds_read_b128 v[14:17], v179 offset:2048
	ds_read_b128 v[194:197], v180
	ds_read_b128 v[202:205], v180 offset:2048
	ds_read_b128 v[198:201], v181
	ds_read_b128 v[206:209], v181 offset:2048
	ds_read_b128 v[210:213], v180 offset:4096
	ds_read_b128 v[218:221], v180 offset:6144
	ds_read_b128 v[214:217], v181 offset:4096
	ds_read_b128 v[222:225], v181 offset:6144
	s_add_u32 s64, s12, s4
	s_addc_u32 s65, s13, s5
	s_add_u32 s46, s64, 0x80
	s_addc_u32 s47, s65, 0
	s_mov_b32 m0, s58
	s_nop 0
	global_load_lds_dwordx4 v163, s[46:47] offset:0 nt
	s_nop 0
	s_mov_b32 m0, s59
	s_nop 0
	global_load_lds_dwordx4 v171, s[46:47] offset:0 nt
	s_waitcnt vmcnt(8)
	s_waitcnt lgkmcnt(0)
	s_barrier
	s_setprio 1
	s_waitcnt lgkmcnt(0)
	v_mfma_f32_16x16x128_f8f6f4 v[158:161], v[18:25], v[194:201], 0
	v_mfma_f32_16x16x128_f8f6f4 v[154:157], v[26:33], v[194:201], 0
	v_mfma_f32_16x16x128_f8f6f4 v[142:145], v[18:25], v[202:209], 0
	v_mfma_f32_16x16x128_f8f6f4 v[138:141], v[26:33], v[202:209], 0
	v_mfma_f32_16x16x128_f8f6f4 v[126:129], v[18:25], v[210:217], 0
	v_mfma_f32_16x16x128_f8f6f4 v[122:125], v[26:33], v[210:217], 0
	v_mfma_f32_16x16x128_f8f6f4 v[110:113], v[18:25], v[218:225], 0
	v_mfma_f32_16x16x128_f8f6f4 v[106:109], v[26:33], v[218:225], 0
	s_setprio 0
	s_setprio 1
	v_mfma_f32_16x16x128_f8f6f4 v[150:153], v[2:9], v[194:201], 0
	v_mfma_f32_16x16x128_f8f6f4 v[146:149], v[10:17], v[194:201], 0
	v_mfma_f32_16x16x128_f8f6f4 v[134:137], v[2:9], v[202:209], 0
	v_mfma_f32_16x16x128_f8f6f4 v[130:133], v[10:17], v[202:209], 0
	v_mfma_f32_16x16x128_f8f6f4 v[118:121], v[2:9], v[210:217], 0
	v_mfma_f32_16x16x128_f8f6f4 v[114:117], v[10:17], v[210:217], 0
	v_mfma_f32_16x16x128_f8f6f4 v[102:105], v[2:9], v[218:225], 0
	v_mfma_f32_16x16x128_f8f6f4 v[98:101], v[10:17], v[218:225], 0
	s_setprio 0
	s_barrier
	s_add_u32 s66, s42, s4
	s_addc_u32 s67, s43, s5
	ds_read_b128 v[194:197], v180 offset:16384
	ds_read_b128 v[202:205], v180 offset:18432
	ds_read_b128 v[198:201], v181 offset:16384
	ds_read_b128 v[206:209], v181 offset:18432
	ds_read_b128 v[210:213], v180 offset:20480
	ds_read_b128 v[218:221], v180 offset:22528
	ds_read_b128 v[214:217], v181 offset:20480
	ds_read_b128 v[222:225], v181 offset:22528
	s_add_u32 s46, s66, 0x100
	s_addc_u32 s47, s67, 0
	s_mov_b32 m0, s33
	s_nop 0
	global_load_lds_dwordx4 v172, s[46:47] offset:0
	s_nop 0
	s_mov_b32 m0, s39
	s_nop 0
	global_load_lds_dwordx4 v173, s[46:47] offset:0
	s_add_u32 s46, s66, 0x20100
	s_addc_u32 s47, s67, 0
	s_mov_b32 m0, s41
	s_nop 0
	global_load_lds_dwordx4 v172, s[46:47] offset:0
	s_nop 0
	s_mov_b32 m0, s48
	s_nop 0
	global_load_lds_dwordx4 v173, s[46:47] offset:0
	s_add_u32 s46, s64, 0x100
	s_addc_u32 s47, s65, 0
	s_mov_b32 m0, s1
	s_nop 0
	global_load_lds_dwordx4 v162, s[46:47] offset:0 nt
	s_nop 0
	s_mov_b32 m0, s49
	s_nop 0
	global_load_lds_dwordx4 v170, s[46:47] offset:0 nt
	s_waitcnt vmcnt(8)
	s_waitcnt lgkmcnt(0)
	s_barrier
	s_setprio 1
	s_waitcnt lgkmcnt(5)
	v_mfma_f32_16x16x128_f8f6f4 v[94:97], v[18:25], v[194:201], 0
	v_mfma_f32_16x16x128_f8f6f4 v[90:93], v[26:33], v[194:201], 0
	s_waitcnt lgkmcnt(4)
	v_mfma_f32_16x16x128_f8f6f4 v[78:81], v[18:25], v[202:209], 0
	v_mfma_f32_16x16x128_f8f6f4 v[74:77], v[26:33], v[202:209], 0
	s_waitcnt lgkmcnt(1)
	v_mfma_f32_16x16x128_f8f6f4 v[62:65], v[18:25], v[210:217], 0
	v_mfma_f32_16x16x128_f8f6f4 v[58:61], v[26:33], v[210:217], 0
	s_waitcnt lgkmcnt(0)
	v_mfma_f32_16x16x128_f8f6f4 v[46:49], v[18:25], v[218:225], 0
	v_mfma_f32_16x16x128_f8f6f4 v[42:45], v[26:33], v[218:225], 0
	s_setprio 0
	s_setprio 1
	v_mfma_f32_16x16x128_f8f6f4 v[86:89], v[2:9], v[194:201], 0
	v_mfma_f32_16x16x128_f8f6f4 v[82:85], v[10:17], v[194:201], 0
	v_mfma_f32_16x16x128_f8f6f4 v[70:73], v[2:9], v[202:209], 0
	v_mfma_f32_16x16x128_f8f6f4 v[66:69], v[10:17], v[202:209], 0
	v_mfma_f32_16x16x128_f8f6f4 v[54:57], v[2:9], v[210:217], 0
	v_mfma_f32_16x16x128_f8f6f4 v[50:53], v[10:17], v[210:217], 0
	v_mfma_f32_16x16x128_f8f6f4 v[38:41], v[2:9], v[218:225], 0
	v_mfma_f32_16x16x128_f8f6f4 v[34:37], v[10:17], v[218:225], 0
	s_setprio 0
	s_barrier
	s_add_i32 s68, 0, 0x18000
	v_add_u32_e32 v183, s68, v174
	v_add_u32_e32 v184, s68, v175
	s_add_i32 s68, 0, 0x1c000
	v_add_u32_e32 v185, s68, v174
	ds_read_b128 v[2:5], v183
	ds_read_b128 v[10:13], v183 offset:2048
	ds_read_b128 v[6:9], v184
	ds_read_b128 v[14:17], v184 offset:2048
	v_add_u32_e32 v186, s68, v175
	ds_read_b128 v[18:21], v185
	ds_read_b128 v[26:29], v185 offset:2048
	ds_read_b128 v[22:25], v186
	ds_read_b128 v[30:33], v186 offset:2048
	ds_read_b128 v[194:197], v180 offset:32768
	ds_read_b128 v[202:205], v180 offset:34816
	ds_read_b128 v[198:201], v181 offset:32768
	ds_read_b128 v[206:209], v181 offset:34816
	ds_read_b128 v[210:213], v180 offset:36864
	ds_read_b128 v[218:221], v180 offset:38912
	ds_read_b128 v[214:217], v181 offset:36864
	ds_read_b128 v[222:225], v181 offset:38912
	s_mov_b32 m0, s50
	s_nop 0
	global_load_lds_dwordx4 v163, s[46:47] offset:0 nt
	s_nop 0
	s_mov_b32 m0, s51
	s_nop 0
	global_load_lds_dwordx4 v171, s[46:47] offset:0 nt
	s_waitcnt vmcnt(8)
	s_waitcnt lgkmcnt(0)
	s_barrier
	s_setprio 1
	s_waitcnt lgkmcnt(5)
	v_mfma_f32_16x16x128_f8f6f4 v[158:161], v[2:9], v[194:201], v[158:161]
	v_mfma_f32_16x16x128_f8f6f4 v[154:157], v[10:17], v[194:201], v[154:157]
	s_waitcnt lgkmcnt(4)
	v_mfma_f32_16x16x128_f8f6f4 v[142:145], v[2:9], v[202:209], v[142:145]
	v_mfma_f32_16x16x128_f8f6f4 v[138:141], v[10:17], v[202:209], v[138:141]
	s_waitcnt lgkmcnt(1)
	v_mfma_f32_16x16x128_f8f6f4 v[126:129], v[2:9], v[210:217], v[126:129]
	v_mfma_f32_16x16x128_f8f6f4 v[122:125], v[10:17], v[210:217], v[122:125]
	s_waitcnt lgkmcnt(0)
	v_mfma_f32_16x16x128_f8f6f4 v[110:113], v[2:9], v[218:225], v[110:113]
	v_mfma_f32_16x16x128_f8f6f4 v[106:109], v[10:17], v[218:225], v[106:109]
	s_setprio 0
	s_setprio 1
	v_mfma_f32_16x16x128_f8f6f4 v[150:153], v[18:25], v[194:201], v[150:153]
	v_mfma_f32_16x16x128_f8f6f4 v[146:149], v[26:33], v[194:201], v[146:149]
	v_mfma_f32_16x16x128_f8f6f4 v[134:137], v[18:25], v[202:209], v[134:137]
	v_mfma_f32_16x16x128_f8f6f4 v[130:133], v[26:33], v[202:209], v[130:133]
	v_mfma_f32_16x16x128_f8f6f4 v[118:121], v[18:25], v[210:217], v[118:121]
	v_mfma_f32_16x16x128_f8f6f4 v[114:117], v[26:33], v[210:217], v[114:117]
	v_mfma_f32_16x16x128_f8f6f4 v[102:105], v[18:25], v[218:225], v[102:105]
	v_mfma_f32_16x16x128_f8f6f4 v[98:101], v[26:33], v[218:225], v[98:101]
	s_setprio 0
	s_barrier
	ds_read_b128 v[194:197], v180 offset:49152
	ds_read_b128 v[202:205], v180 offset:51200
	ds_read_b128 v[198:201], v181 offset:49152
	ds_read_b128 v[206:209], v181 offset:51200
	ds_read_b128 v[210:213], v180 offset:53248
	ds_read_b128 v[218:221], v180 offset:55296
	ds_read_b128 v[214:217], v181 offset:53248
	ds_read_b128 v[222:225], v181 offset:55296
	s_add_u32 s46, s66, 0x180
	s_addc_u32 s47, s67, 0
	s_mov_b32 m0, s52
	s_nop 0
	global_load_lds_dwordx4 v172, s[46:47] offset:0
	s_nop 0
	s_mov_b32 m0, s53
	s_nop 0
	global_load_lds_dwordx4 v173, s[46:47] offset:0
	s_add_u32 s46, s66, 0x20180
	s_addc_u32 s47, s67, 0
	s_mov_b32 m0, s56
	s_nop 0
	global_load_lds_dwordx4 v172, s[46:47] offset:0
	s_nop 0
	s_mov_b32 m0, s57
	s_nop 0
	global_load_lds_dwordx4 v173, s[46:47] offset:0
	s_add_u32 s46, s64, 0x180
	s_addc_u32 s47, s65, 0
	s_mov_b32 m0, s54
	s_nop 0
	global_load_lds_dwordx4 v162, s[46:47] offset:0 nt
	s_nop 0
	s_mov_b32 m0, s55
	s_nop 0
	global_load_lds_dwordx4 v170, s[46:47] offset:0 nt
	s_waitcnt vmcnt(8)
	s_waitcnt lgkmcnt(0)
	s_barrier
	s_setprio 1
	s_waitcnt lgkmcnt(5)
	v_mfma_f32_16x16x128_f8f6f4 v[94:97], v[2:9], v[194:201], v[94:97]
	v_mfma_f32_16x16x128_f8f6f4 v[90:93], v[10:17], v[194:201], v[90:93]
	s_waitcnt lgkmcnt(4)
	v_mfma_f32_16x16x128_f8f6f4 v[78:81], v[2:9], v[202:209], v[78:81]
	v_mfma_f32_16x16x128_f8f6f4 v[74:77], v[10:17], v[202:209], v[74:77]
	s_waitcnt lgkmcnt(1)
	v_mfma_f32_16x16x128_f8f6f4 v[62:65], v[2:9], v[210:217], v[62:65]
	v_mfma_f32_16x16x128_f8f6f4 v[58:61], v[10:17], v[210:217], v[58:61]
	s_waitcnt lgkmcnt(0)
	v_mfma_f32_16x16x128_f8f6f4 v[46:49], v[2:9], v[218:225], v[46:49]
	v_mfma_f32_16x16x128_f8f6f4 v[42:45], v[10:17], v[218:225], v[42:45]
	s_setprio 0
	s_setprio 1
	v_mfma_f32_16x16x128_f8f6f4 v[86:89], v[18:25], v[194:201], v[86:89]
	v_mfma_f32_16x16x128_f8f6f4 v[82:85], v[26:33], v[194:201], v[82:85]
	v_mfma_f32_16x16x128_f8f6f4 v[70:73], v[18:25], v[202:209], v[70:73]
	v_mfma_f32_16x16x128_f8f6f4 v[66:69], v[26:33], v[202:209], v[66:69]
	v_mfma_f32_16x16x128_f8f6f4 v[54:57], v[18:25], v[210:217], v[54:57]
	v_mfma_f32_16x16x128_f8f6f4 v[50:53], v[26:33], v[210:217], v[50:53]
	v_mfma_f32_16x16x128_f8f6f4 v[38:41], v[18:25], v[218:225], v[38:41]
	v_mfma_f32_16x16x128_f8f6f4 v[34:37], v[26:33], v[218:225], v[34:37]
	s_setprio 0
	s_add_i32 s35, s35, 2
	s_add_u32 s4, s4, 0x100
	s_addc_u32 s5, s5, 0
	s_barrier
.LBB0_650:
	.p2align 3
	s_nop 0
	ds_read_b128 v[18:21], v176
	ds_read_b128 v[26:29], v176 offset:2048
	ds_read_b128 v[22:25], v177
	ds_read_b128 v[30:33], v177 offset:2048
	ds_read_b128 v[2:5], v178
	ds_read_b128 v[10:13], v178 offset:2048
	ds_read_b128 v[6:9], v179
	ds_read_b128 v[14:17], v179 offset:2048
	ds_read_b128 v[194:197], v180
	ds_read_b128 v[202:205], v180 offset:2048
	ds_read_b128 v[198:201], v181
	ds_read_b128 v[206:209], v181 offset:2048
	ds_read_b128 v[210:213], v180 offset:4096
	ds_read_b128 v[218:221], v180 offset:6144
	ds_read_b128 v[214:217], v181 offset:4096
	ds_read_b128 v[222:225], v181 offset:6144
	s_add_u32 s64, s12, s4
	s_addc_u32 s65, s13, s5
	s_add_u32 s46, s64, 0x80
	s_addc_u32 s47, s65, 0
	s_mov_b32 m0, s58
	s_nop 0
	global_load_lds_dwordx4 v163, s[46:47] offset:0 nt
	s_nop 0
	s_mov_b32 m0, s59
	s_nop 0
	global_load_lds_dwordx4 v171, s[46:47] offset:0 nt
	s_waitcnt vmcnt(8)
	s_waitcnt lgkmcnt(0)
	s_barrier
	s_setprio 1
	s_waitcnt lgkmcnt(0)
	v_mfma_f32_16x16x128_f8f6f4 v[158:161], v[18:25], v[194:201], v[158:161]
	v_mfma_f32_16x16x128_f8f6f4 v[154:157], v[26:33], v[194:201], v[154:157]
	v_mfma_f32_16x16x128_f8f6f4 v[142:145], v[18:25], v[202:209], v[142:145]
	v_mfma_f32_16x16x128_f8f6f4 v[138:141], v[26:33], v[202:209], v[138:141]
	v_mfma_f32_16x16x128_f8f6f4 v[126:129], v[18:25], v[210:217], v[126:129]
	v_mfma_f32_16x16x128_f8f6f4 v[122:125], v[26:33], v[210:217], v[122:125]
	v_mfma_f32_16x16x128_f8f6f4 v[110:113], v[18:25], v[218:225], v[110:113]
	v_mfma_f32_16x16x128_f8f6f4 v[106:109], v[26:33], v[218:225], v[106:109]
	s_setprio 0
	s_setprio 1
	v_mfma_f32_16x16x128_f8f6f4 v[150:153], v[2:9], v[194:201], v[150:153]
	v_mfma_f32_16x16x128_f8f6f4 v[146:149], v[10:17], v[194:201], v[146:149]
	v_mfma_f32_16x16x128_f8f6f4 v[134:137], v[2:9], v[202:209], v[134:137]
	v_mfma_f32_16x16x128_f8f6f4 v[130:133], v[10:17], v[202:209], v[130:133]
	v_mfma_f32_16x16x128_f8f6f4 v[118:121], v[2:9], v[210:217], v[118:121]
	v_mfma_f32_16x16x128_f8f6f4 v[114:117], v[10:17], v[210:217], v[114:117]
	v_mfma_f32_16x16x128_f8f6f4 v[102:105], v[2:9], v[218:225], v[102:105]
	v_mfma_f32_16x16x128_f8f6f4 v[98:101], v[10:17], v[218:225], v[98:101]
	s_setprio 0
	s_barrier
	s_add_u32 s66, s42, s4
	s_addc_u32 s67, s43, s5
	ds_read_b128 v[194:197], v180 offset:16384
	ds_read_b128 v[202:205], v180 offset:18432
	ds_read_b128 v[198:201], v181 offset:16384
	ds_read_b128 v[206:209], v181 offset:18432
	ds_read_b128 v[210:213], v180 offset:20480
	ds_read_b128 v[218:221], v180 offset:22528
	ds_read_b128 v[214:217], v181 offset:20480
	ds_read_b128 v[222:225], v181 offset:22528
	s_add_u32 s46, s66, 0x100
	s_addc_u32 s47, s67, 0
	s_mov_b32 m0, s33
	s_nop 0
	global_load_lds_dwordx4 v172, s[46:47] offset:0
	s_nop 0
	s_mov_b32 m0, s39
	s_nop 0
	global_load_lds_dwordx4 v173, s[46:47] offset:0
	s_add_u32 s46, s66, 0x20100
	s_addc_u32 s47, s67, 0
	s_mov_b32 m0, s41
	s_nop 0
	global_load_lds_dwordx4 v172, s[46:47] offset:0
	s_nop 0
	s_mov_b32 m0, s48
	s_nop 0
	global_load_lds_dwordx4 v173, s[46:47] offset:0
	s_add_u32 s46, s64, 0x100
	s_addc_u32 s47, s65, 0
	s_mov_b32 m0, s1
	s_nop 0
	global_load_lds_dwordx4 v162, s[46:47] offset:0 nt
	s_nop 0
	s_mov_b32 m0, s49
	s_nop 0
	global_load_lds_dwordx4 v170, s[46:47] offset:0 nt
	s_waitcnt vmcnt(8)
	s_waitcnt lgkmcnt(0)
	s_barrier
	s_setprio 1
	s_waitcnt lgkmcnt(5)
	v_mfma_f32_16x16x128_f8f6f4 v[94:97], v[18:25], v[194:201], v[94:97]
	v_mfma_f32_16x16x128_f8f6f4 v[90:93], v[26:33], v[194:201], v[90:93]
	s_waitcnt lgkmcnt(4)
	v_mfma_f32_16x16x128_f8f6f4 v[78:81], v[18:25], v[202:209], v[78:81]
	v_mfma_f32_16x16x128_f8f6f4 v[74:77], v[26:33], v[202:209], v[74:77]
	s_waitcnt lgkmcnt(1)
	v_mfma_f32_16x16x128_f8f6f4 v[62:65], v[18:25], v[210:217], v[62:65]
	v_mfma_f32_16x16x128_f8f6f4 v[58:61], v[26:33], v[210:217], v[58:61]
	s_waitcnt lgkmcnt(0)
	v_mfma_f32_16x16x128_f8f6f4 v[46:49], v[18:25], v[218:225], v[46:49]
	v_mfma_f32_16x16x128_f8f6f4 v[42:45], v[26:33], v[218:225], v[42:45]
	s_setprio 0
	s_setprio 1
	v_mfma_f32_16x16x128_f8f6f4 v[86:89], v[2:9], v[194:201], v[86:89]
	v_mfma_f32_16x16x128_f8f6f4 v[82:85], v[10:17], v[194:201], v[82:85]
	v_mfma_f32_16x16x128_f8f6f4 v[70:73], v[2:9], v[202:209], v[70:73]
	v_mfma_f32_16x16x128_f8f6f4 v[66:69], v[10:17], v[202:209], v[66:69]
	v_mfma_f32_16x16x128_f8f6f4 v[54:57], v[2:9], v[210:217], v[54:57]
	v_mfma_f32_16x16x128_f8f6f4 v[50:53], v[10:17], v[210:217], v[50:53]
	v_mfma_f32_16x16x128_f8f6f4 v[38:41], v[2:9], v[218:225], v[38:41]
	v_mfma_f32_16x16x128_f8f6f4 v[34:37], v[10:17], v[218:225], v[34:37]
	s_setprio 0
	s_barrier
	s_add_i32 s68, 0, 0x18000
	v_add_u32_e32 v183, s68, v174
	v_add_u32_e32 v184, s68, v175
	s_add_i32 s68, 0, 0x1c000
	v_add_u32_e32 v185, s68, v174
	ds_read_b128 v[2:5], v183
	ds_read_b128 v[10:13], v183 offset:2048
	ds_read_b128 v[6:9], v184
	ds_read_b128 v[14:17], v184 offset:2048
	v_add_u32_e32 v186, s68, v175
	ds_read_b128 v[18:21], v185
	ds_read_b128 v[26:29], v185 offset:2048
	ds_read_b128 v[22:25], v186
	ds_read_b128 v[30:33], v186 offset:2048
	ds_read_b128 v[194:197], v180 offset:32768
	ds_read_b128 v[202:205], v180 offset:34816
	ds_read_b128 v[198:201], v181 offset:32768
	ds_read_b128 v[206:209], v181 offset:34816
	ds_read_b128 v[210:213], v180 offset:36864
	ds_read_b128 v[218:221], v180 offset:38912
	ds_read_b128 v[214:217], v181 offset:36864
	ds_read_b128 v[222:225], v181 offset:38912
	s_mov_b32 m0, s50
	s_nop 0
	global_load_lds_dwordx4 v163, s[46:47] offset:0 nt
	s_nop 0
	s_mov_b32 m0, s51
	s_nop 0
	global_load_lds_dwordx4 v171, s[46:47] offset:0 nt
	s_waitcnt vmcnt(8)
	s_waitcnt lgkmcnt(0)
	s_barrier
	s_setprio 1
	s_waitcnt lgkmcnt(5)
	v_mfma_f32_16x16x128_f8f6f4 v[158:161], v[2:9], v[194:201], v[158:161]
	v_mfma_f32_16x16x128_f8f6f4 v[154:157], v[10:17], v[194:201], v[154:157]
	s_waitcnt lgkmcnt(4)
	v_mfma_f32_16x16x128_f8f6f4 v[142:145], v[2:9], v[202:209], v[142:145]
	v_mfma_f32_16x16x128_f8f6f4 v[138:141], v[10:17], v[202:209], v[138:141]
	s_waitcnt lgkmcnt(1)
	v_mfma_f32_16x16x128_f8f6f4 v[126:129], v[2:9], v[210:217], v[126:129]
	v_mfma_f32_16x16x128_f8f6f4 v[122:125], v[10:17], v[210:217], v[122:125]
	s_waitcnt lgkmcnt(0)
	v_mfma_f32_16x16x128_f8f6f4 v[110:113], v[2:9], v[218:225], v[110:113]
	v_mfma_f32_16x16x128_f8f6f4 v[106:109], v[10:17], v[218:225], v[106:109]
	s_setprio 0
	s_setprio 1
	v_mfma_f32_16x16x128_f8f6f4 v[150:153], v[18:25], v[194:201], v[150:153]
	v_mfma_f32_16x16x128_f8f6f4 v[146:149], v[26:33], v[194:201], v[146:149]
	v_mfma_f32_16x16x128_f8f6f4 v[134:137], v[18:25], v[202:209], v[134:137]
	v_mfma_f32_16x16x128_f8f6f4 v[130:133], v[26:33], v[202:209], v[130:133]
	v_mfma_f32_16x16x128_f8f6f4 v[118:121], v[18:25], v[210:217], v[118:121]
	v_mfma_f32_16x16x128_f8f6f4 v[114:117], v[26:33], v[210:217], v[114:117]
	v_mfma_f32_16x16x128_f8f6f4 v[102:105], v[18:25], v[218:225], v[102:105]
	v_mfma_f32_16x16x128_f8f6f4 v[98:101], v[26:33], v[218:225], v[98:101]
	s_setprio 0
	s_barrier
	ds_read_b128 v[194:197], v180 offset:49152
	ds_read_b128 v[202:205], v180 offset:51200
	ds_read_b128 v[198:201], v181 offset:49152
	ds_read_b128 v[206:209], v181 offset:51200
	ds_read_b128 v[210:213], v180 offset:53248
	ds_read_b128 v[218:221], v180 offset:55296
	ds_read_b128 v[214:217], v181 offset:53248
	ds_read_b128 v[222:225], v181 offset:55296
	s_add_u32 s46, s66, 0x180
	s_addc_u32 s47, s67, 0
	s_mov_b32 m0, s52
	s_nop 0
	global_load_lds_dwordx4 v172, s[46:47] offset:0
	s_nop 0
	s_mov_b32 m0, s53
	s_nop 0
	global_load_lds_dwordx4 v173, s[46:47] offset:0
	s_add_u32 s46, s66, 0x20180
	s_addc_u32 s47, s67, 0
	s_mov_b32 m0, s56
	s_nop 0
	global_load_lds_dwordx4 v172, s[46:47] offset:0
	s_nop 0
	s_mov_b32 m0, s57
	s_nop 0
	global_load_lds_dwordx4 v173, s[46:47] offset:0
	s_add_u32 s46, s64, 0x180
	s_addc_u32 s47, s65, 0
	s_mov_b32 m0, s54
	s_nop 0
	global_load_lds_dwordx4 v162, s[46:47] offset:0 nt
	s_nop 0
	s_mov_b32 m0, s55
	s_nop 0
	global_load_lds_dwordx4 v170, s[46:47] offset:0 nt
	s_waitcnt vmcnt(8)
	s_waitcnt lgkmcnt(0)
	s_barrier
	s_setprio 1
	s_waitcnt lgkmcnt(5)
	v_mfma_f32_16x16x128_f8f6f4 v[94:97], v[2:9], v[194:201], v[94:97]
	v_mfma_f32_16x16x128_f8f6f4 v[90:93], v[10:17], v[194:201], v[90:93]
	s_waitcnt lgkmcnt(4)
	v_mfma_f32_16x16x128_f8f6f4 v[78:81], v[2:9], v[202:209], v[78:81]
	v_mfma_f32_16x16x128_f8f6f4 v[74:77], v[10:17], v[202:209], v[74:77]
	s_waitcnt lgkmcnt(1)
	v_mfma_f32_16x16x128_f8f6f4 v[62:65], v[2:9], v[210:217], v[62:65]
	v_mfma_f32_16x16x128_f8f6f4 v[58:61], v[10:17], v[210:217], v[58:61]
	s_waitcnt lgkmcnt(0)
	v_mfma_f32_16x16x128_f8f6f4 v[46:49], v[2:9], v[218:225], v[46:49]
	v_mfma_f32_16x16x128_f8f6f4 v[42:45], v[10:17], v[218:225], v[42:45]
	s_setprio 0
	s_setprio 1
	v_mfma_f32_16x16x128_f8f6f4 v[86:89], v[18:25], v[194:201], v[86:89]
	v_mfma_f32_16x16x128_f8f6f4 v[82:85], v[26:33], v[194:201], v[82:85]
	v_mfma_f32_16x16x128_f8f6f4 v[70:73], v[18:25], v[202:209], v[70:73]
	v_mfma_f32_16x16x128_f8f6f4 v[66:69], v[26:33], v[202:209], v[66:69]
	v_mfma_f32_16x16x128_f8f6f4 v[54:57], v[18:25], v[210:217], v[54:57]
	v_mfma_f32_16x16x128_f8f6f4 v[50:53], v[26:33], v[210:217], v[50:53]
	v_mfma_f32_16x16x128_f8f6f4 v[38:41], v[18:25], v[218:225], v[38:41]
	v_mfma_f32_16x16x128_f8f6f4 v[34:37], v[26:33], v[218:225], v[34:37]
	s_setprio 0
	s_add_i32 s35, s35, 2
	s_add_u32 s4, s4, 0x100
	s_addc_u32 s5, s5, 0
	s_cmp_lt_u32 s35, 4
	s_barrier
	s_cbranch_scc1 .LBB0_650
	ds_read_b128 v[18:21], v176
	ds_read_b128 v[26:29], v176 offset:2048
	ds_read_b128 v[22:25], v177
	ds_read_b128 v[30:33], v177 offset:2048
	ds_read_b128 v[2:5], v178
	ds_read_b128 v[10:13], v178 offset:2048
	ds_read_b128 v[6:9], v179
	ds_read_b128 v[14:17], v179 offset:2048
	ds_read_b128 v[194:197], v180
	ds_read_b128 v[202:205], v180 offset:2048
	ds_read_b128 v[198:201], v181
	ds_read_b128 v[206:209], v181 offset:2048
	ds_read_b128 v[210:213], v180 offset:4096
	ds_read_b128 v[218:221], v180 offset:6144
	ds_read_b128 v[214:217], v181 offset:4096
	ds_read_b128 v[222:225], v181 offset:6144
	s_mov_b32 m0, s58
	s_nop 0
	global_load_lds_dwordx4 v163, s[24:25] offset:0 nt
	s_nop 0
	s_mov_b32 m0, s59
	s_nop 0
	global_load_lds_dwordx4 v171, s[24:25] offset:0 nt
	s_waitcnt vmcnt(8)
	s_waitcnt lgkmcnt(0)
	s_barrier
	s_setprio 1
	s_waitcnt lgkmcnt(5)
	v_mfma_f32_16x16x128_f8f6f4 v[158:161], v[18:25], v[194:201], v[158:161]
	v_mfma_f32_16x16x128_f8f6f4 v[154:157], v[26:33], v[194:201], v[154:157]
	s_waitcnt lgkmcnt(4)
	v_mfma_f32_16x16x128_f8f6f4 v[142:145], v[18:25], v[202:209], v[142:145]
	v_mfma_f32_16x16x128_f8f6f4 v[138:141], v[26:33], v[202:209], v[138:141]
	s_waitcnt lgkmcnt(1)
	v_mfma_f32_16x16x128_f8f6f4 v[126:129], v[18:25], v[210:217], v[126:129]
	v_mfma_f32_16x16x128_f8f6f4 v[122:125], v[26:33], v[210:217], v[122:125]
	s_waitcnt lgkmcnt(0)
	v_mfma_f32_16x16x128_f8f6f4 v[110:113], v[18:25], v[218:225], v[110:113]
	v_mfma_f32_16x16x128_f8f6f4 v[106:109], v[26:33], v[218:225], v[106:109]
	s_setprio 0
	s_setprio 1
	v_mfma_f32_16x16x128_f8f6f4 v[150:153], v[2:9], v[194:201], v[150:153]
	v_mfma_f32_16x16x128_f8f6f4 v[146:149], v[10:17], v[194:201], v[146:149]
	v_mfma_f32_16x16x128_f8f6f4 v[134:137], v[2:9], v[202:209], v[134:137]
	v_mfma_f32_16x16x128_f8f6f4 v[130:133], v[10:17], v[202:209], v[130:133]
	v_mfma_f32_16x16x128_f8f6f4 v[118:121], v[2:9], v[210:217], v[118:121]
	v_mfma_f32_16x16x128_f8f6f4 v[114:117], v[10:17], v[210:217], v[114:117]
	v_mfma_f32_16x16x128_f8f6f4 v[102:105], v[2:9], v[218:225], v[102:105]
	v_mfma_f32_16x16x128_f8f6f4 v[98:101], v[10:17], v[218:225], v[98:101]
	s_setprio 0
	s_barrier
	v_cndmask_b32_e64 v187, 0, 1, s[44:45]
	v_cmp_ne_u32_e64 s[4:5], 1, v187
	s_andn2_b64 vcc, exec, s[44:45]
	s_cbranch_vccnz .LBB0_653
	v_mov_b32_e32 v162, v0
	s_nop 0
	v_lshlrev_b32_e32 v163, 4, v162
	v_bitop3_b32 v163, v163, s0, v162 bitop3:0x48
	v_lshlrev_b32_e32 v162, 7, v162
	v_lshl_or_b32 v163, s61, 18, v163
	v_and_b32_e32 v162, 0xfffffc00, v162
	v_add_u32_e32 v162, v163, v162
	v_add_u32_e32 v163, 0x20000, v162
	v_add_u32_e32 v170, 0x10000, v162
	v_add_u32_e32 v171, 0x30000, v162
.LBB0_653:
	s_ashr_i32 s35, s34, 31
	s_lshl_b64 s[46:47], s[34:35], 18
	s_add_u32 s46, s29, s46
	s_addc_u32 s47, s31, s47
	s_and_b64 s[44:45], s[44:45], exec
	ds_read_b128 v[194:197], v180 offset:16384
	ds_read_b128 v[202:205], v180 offset:18432
	ds_read_b128 v[198:201], v181 offset:16384
	ds_read_b128 v[206:209], v181 offset:18432
	ds_read_b128 v[210:213], v180 offset:20480
	ds_read_b128 v[218:221], v180 offset:22528
	ds_read_b128 v[214:217], v181 offset:20480
	ds_read_b128 v[222:225], v181 offset:22528
	s_cselect_b32 s43, s47, s43
	s_cselect_b32 s42, s46, s42
	s_mov_b32 m0, s33
	s_nop 0
	global_load_lds_dwordx4 v172, s[42:43] offset:0
	s_add_u32 s44, s42, 0x20000
	s_mov_b32 m0, s39
	s_nop 0
	global_load_lds_dwordx4 v173, s[42:43] offset:0
	s_addc_u32 s45, s43, 0
	s_mov_b32 m0, s41
	s_nop 0
	global_load_lds_dwordx4 v172, s[44:45] offset:0
	s_nop 0
	s_mov_b32 m0, s48
	s_nop 0
	global_load_lds_dwordx4 v173, s[44:45] offset:0
	s_nop 0
	s_mov_b32 m0, s1
	s_nop 0
	global_load_lds_dwordx4 v162, s[12:13] offset:0 nt
	s_nop 0
	s_mov_b32 m0, s49
	s_nop 0
	global_load_lds_dwordx4 v170, s[12:13] offset:0 nt
	s_waitcnt vmcnt(8)
	s_waitcnt lgkmcnt(0)
	s_barrier
	s_setprio 1
	s_waitcnt lgkmcnt(5)
	v_mfma_f32_16x16x128_f8f6f4 v[94:97], v[18:25], v[194:201], v[94:97]
	v_mfma_f32_16x16x128_f8f6f4 v[90:93], v[26:33], v[194:201], v[90:93]
	s_waitcnt lgkmcnt(4)
	v_mfma_f32_16x16x128_f8f6f4 v[78:81], v[18:25], v[202:209], v[78:81]
	v_mfma_f32_16x16x128_f8f6f4 v[74:77], v[26:33], v[202:209], v[74:77]
	s_waitcnt lgkmcnt(1)
	v_mfma_f32_16x16x128_f8f6f4 v[62:65], v[18:25], v[210:217], v[62:65]
	v_mfma_f32_16x16x128_f8f6f4 v[58:61], v[26:33], v[210:217], v[58:61]
	s_waitcnt lgkmcnt(0)
	v_mfma_f32_16x16x128_f8f6f4 v[46:49], v[18:25], v[218:225], v[46:49]
	v_mfma_f32_16x16x128_f8f6f4 v[42:45], v[26:33], v[218:225], v[42:45]
	s_setprio 0
	s_setprio 1
	v_mfma_f32_16x16x128_f8f6f4 v[86:89], v[2:9], v[194:201], v[86:89]
	v_mfma_f32_16x16x128_f8f6f4 v[82:85], v[10:17], v[194:201], v[82:85]
	v_mfma_f32_16x16x128_f8f6f4 v[70:73], v[2:9], v[202:209], v[70:73]
	v_mfma_f32_16x16x128_f8f6f4 v[66:69], v[10:17], v[202:209], v[66:69]
	v_mfma_f32_16x16x128_f8f6f4 v[54:57], v[2:9], v[210:217], v[54:57]
	v_mfma_f32_16x16x128_f8f6f4 v[50:53], v[10:17], v[210:217], v[50:53]
	v_mfma_f32_16x16x128_f8f6f4 v[38:41], v[2:9], v[218:225], v[38:41]
	v_mfma_f32_16x16x128_f8f6f4 v[34:37], v[10:17], v[218:225], v[34:37]
	s_setprio 0
	s_barrier
	ds_read_b128 v[2:5], v183
	ds_read_b128 v[10:13], v183 offset:2048
	ds_read_b128 v[6:9], v184
	ds_read_b128 v[14:17], v184 offset:2048
	ds_read_b128 v[18:21], v185
	ds_read_b128 v[26:29], v185 offset:2048
	ds_read_b128 v[22:25], v186
	ds_read_b128 v[30:33], v186 offset:2048
	ds_read_b128 v[194:197], v180 offset:32768
	ds_read_b128 v[202:205], v180 offset:34816
	ds_read_b128 v[198:201], v181 offset:32768
	ds_read_b128 v[206:209], v181 offset:34816
	ds_read_b128 v[210:213], v180 offset:36864
	ds_read_b128 v[218:221], v180 offset:38912
	ds_read_b128 v[214:217], v181 offset:36864
	ds_read_b128 v[222:225], v181 offset:38912
	s_mov_b32 m0, s50
	s_nop 0
	global_load_lds_dwordx4 v163, s[12:13] offset:0 nt
	s_nop 0
	s_mov_b32 m0, s51
	s_nop 0
	global_load_lds_dwordx4 v171, s[12:13] offset:0 nt
	s_waitcnt vmcnt(8)
	s_waitcnt lgkmcnt(0)
	s_barrier
	s_setprio 1
	s_waitcnt lgkmcnt(5)
	v_mfma_f32_16x16x128_f8f6f4 v[158:161], v[2:9], v[194:201], v[158:161]
	v_mfma_f32_16x16x128_f8f6f4 v[154:157], v[10:17], v[194:201], v[154:157]
	s_waitcnt lgkmcnt(4)
	v_mfma_f32_16x16x128_f8f6f4 v[142:145], v[2:9], v[202:209], v[142:145]
	v_mfma_f32_16x16x128_f8f6f4 v[138:141], v[10:17], v[202:209], v[138:141]
	s_waitcnt lgkmcnt(1)
	v_mfma_f32_16x16x128_f8f6f4 v[126:129], v[2:9], v[210:217], v[126:129]
	v_mfma_f32_16x16x128_f8f6f4 v[122:125], v[10:17], v[210:217], v[122:125]
	s_waitcnt lgkmcnt(0)
	v_mfma_f32_16x16x128_f8f6f4 v[110:113], v[2:9], v[218:225], v[110:113]
	v_mfma_f32_16x16x128_f8f6f4 v[106:109], v[10:17], v[218:225], v[106:109]
	s_setprio 0
	s_setprio 1
	v_mfma_f32_16x16x128_f8f6f4 v[150:153], v[18:25], v[194:201], v[150:153]
	v_mfma_f32_16x16x128_f8f6f4 v[146:149], v[26:33], v[194:201], v[146:149]
	v_mfma_f32_16x16x128_f8f6f4 v[134:137], v[18:25], v[202:209], v[134:137]
	v_mfma_f32_16x16x128_f8f6f4 v[130:133], v[26:33], v[202:209], v[130:133]
	v_mfma_f32_16x16x128_f8f6f4 v[118:121], v[18:25], v[210:217], v[118:121]
	v_mfma_f32_16x16x128_f8f6f4 v[114:117], v[26:33], v[210:217], v[114:117]
	v_mfma_f32_16x16x128_f8f6f4 v[102:105], v[18:25], v[218:225], v[102:105]
	v_mfma_f32_16x16x128_f8f6f4 v[98:101], v[26:33], v[218:225], v[98:101]
	s_setprio 0
	s_barrier
	ds_read_b128 v[194:197], v180 offset:49152
	ds_read_b128 v[202:205], v180 offset:51200
	ds_read_b128 v[198:201], v181 offset:49152
	ds_read_b128 v[206:209], v181 offset:51200
	ds_read_b128 v[210:213], v180 offset:53248
	ds_read_b128 v[218:221], v180 offset:55296
	ds_read_b128 v[214:217], v181 offset:53248
	ds_read_b128 v[222:225], v181 offset:55296
	s_add_u32 s44, s42, 0x80
	s_addc_u32 s45, s43, 0
	s_mov_b32 m0, s52
	s_nop 0
	global_load_lds_dwordx4 v172, s[44:45] offset:0
	s_add_u32 s42, s42, 0x20080
	s_mov_b32 m0, s53
	s_nop 0
	global_load_lds_dwordx4 v173, s[44:45] offset:0
	s_addc_u32 s43, s43, 0
	s_mov_b32 m0, s56
	s_nop 0
	global_load_lds_dwordx4 v172, s[42:43] offset:0
	s_nop 0
	s_mov_b32 m0, s57
	s_nop 0
	global_load_lds_dwordx4 v173, s[42:43] offset:0
	s_nop 0
	s_mov_b32 m0, s54
	s_nop 0
	global_load_lds_dwordx4 v162, s[22:23] offset:0 nt
	s_nop 0
	s_mov_b32 m0, s55
	s_nop 0
	global_load_lds_dwordx4 v170, s[22:23] offset:0 nt
	s_waitcnt vmcnt(8)
	s_waitcnt lgkmcnt(0)
	s_barrier
	s_setprio 1
	s_waitcnt lgkmcnt(5)
	v_mfma_f32_16x16x128_f8f6f4 v[94:97], v[2:9], v[194:201], v[94:97]
	v_mfma_f32_16x16x128_f8f6f4 v[90:93], v[10:17], v[194:201], v[90:93]
	s_waitcnt lgkmcnt(4)
	v_mfma_f32_16x16x128_f8f6f4 v[78:81], v[2:9], v[202:209], v[78:81]
	v_mfma_f32_16x16x128_f8f6f4 v[74:77], v[10:17], v[202:209], v[74:77]
	s_waitcnt lgkmcnt(1)
	v_mfma_f32_16x16x128_f8f6f4 v[62:65], v[2:9], v[210:217], v[62:65]
	v_mfma_f32_16x16x128_f8f6f4 v[58:61], v[10:17], v[210:217], v[58:61]
	s_waitcnt lgkmcnt(0)
	v_mfma_f32_16x16x128_f8f6f4 v[46:49], v[2:9], v[218:225], v[46:49]
	v_mfma_f32_16x16x128_f8f6f4 v[42:45], v[10:17], v[218:225], v[42:45]
	s_setprio 0
	s_setprio 1
	v_mfma_f32_16x16x128_f8f6f4 v[86:89], v[18:25], v[194:201], v[86:89]
	v_mfma_f32_16x16x128_f8f6f4 v[82:85], v[26:33], v[194:201], v[82:85]
	v_mfma_f32_16x16x128_f8f6f4 v[70:73], v[18:25], v[202:209], v[70:73]
	v_mfma_f32_16x16x128_f8f6f4 v[66:69], v[26:33], v[202:209], v[66:69]
	v_mfma_f32_16x16x128_f8f6f4 v[54:57], v[18:25], v[210:217], v[54:57]
	v_mfma_f32_16x16x128_f8f6f4 v[50:53], v[26:33], v[210:217], v[50:53]
	v_mfma_f32_16x16x128_f8f6f4 v[38:41], v[18:25], v[218:225], v[38:41]
	v_mfma_f32_16x16x128_f8f6f4 v[34:37], v[26:33], v[218:225], v[34:37]
	s_setprio 0
	s_barrier
	s_nop 15
	s_nop 15
	s_andn2_b64 vcc, exec, s[26:27]
	s_cbranch_vccnz .LBB0_655
	s_barrier
